# host 4096 layer-1 weight-conversion blocks inside the G2_0 routed GEMM unit loop (16 per WG at slot-staggered unit boundary), ATT1 keeps 8192
# baseline (speedup 1.0000x reference)
.LBB0_1053:
	s_lshr_b32 vcc_lo, s2, 3
	s_and_b32 vcc_lo, vcc_lo, 15
	s_cmp_lg_u32 s72, vcc_lo
	s_cbranch_scc1 .Ltg11_skip
	s_waitcnt vmcnt(0)
	v_writelane_b32 v254, s4, 20
	v_writelane_b32 v254, s5, 21
	v_writelane_b32 v254, s6, 22
	v_writelane_b32 v254, s7, 23
	v_writelane_b32 v254, s18, 24
	v_writelane_b32 v254, s19, 25
	v_writelane_b32 v254, s33, 26
	v_writelane_b32 v254, s36, 27
	v_writelane_b32 v254, s38, 28
	v_writelane_b32 v254, s39, 29
	v_writelane_b32 v254, s40, 30
	v_writelane_b32 v254, s41, 31
	v_writelane_b32 v254, s42, 32
	v_writelane_b32 v254, s43, 33
	v_writelane_b32 v254, s44, 34
	v_writelane_b32 v254, s45, 35
	v_writelane_b32 v254, s46, 36
	v_writelane_b32 v254, s47, 37
	v_writelane_b32 v254, s48, 38
	v_writelane_b32 v254, s49, 39
	v_writelane_b32 v254, s50, 40
	v_writelane_b32 v254, s51, 41
	v_writelane_b32 v254, s52, 42
	v_writelane_b32 v254, s53, 43
	v_writelane_b32 v254, s54, 44
	v_writelane_b32 v254, s55, 45
	v_writelane_b32 v254, s56, 46
	v_writelane_b32 v254, s57, 47
	v_writelane_b32 v254, s58, 48
	v_writelane_b32 v254, s59, 49
	v_writelane_b32 v254, s60, 50
	v_writelane_b32 v254, s61, 51
	s_mul_i32 s60, s2, 16
	s_add_i32 s60, s60, 0x2000
	s_add_i32 s61, s60, 16
	v_readlane_b32 s38, v254, 0
	v_readlane_b32 s39, v254, 1
	s_mov_b32 s7, s95
	v_mbcnt_hi_u32_b32 v200, -1, v194
	s_nop 4
	s_load_dwordx2 s[40:41], s[38:39], 0xb0
	s_load_dwordx2 s[42:43], s[38:39], 0xb8
	s_load_dwordx2 s[44:45], s[38:39], 0xc0
	s_load_dwordx2 s[46:47], s[38:39], 0xe8
	s_lshr_b32 s7, s7, 6
	s_lshr_b32 s48, s7, 2
	s_and_b32 s7, s7, 3
	s_lshl_b32 s7, s7, 3
	v_and_b32_e32 v201, 7, v200
	v_lshrrev_b32_e32 v202, 3, v200
	v_add_u32_e32 v202, s7, v202
	v_lshlrev_b32_e32 v203, 4, v202
	v_lshl_add_u32 v196, v201, 15, v203
	v_lshl_add_u32 v197, v201, 17, v203
	v_lshlrev_b32_e32 v204, 4, v201
	v_lshl_add_u32 v199, v202, 11, v204
	v_lshrrev_b32_e32 v203, 1, v202
	v_and_b32_e32 v205, 1, v202
	v_lshl_add_u32 v198, v203, 15, v204
	v_lshl_add_u32 v198, v205, 13, v198
	v_mov_b32_e32 v195, 0x43dc0000
	s_mov_b32 s6, 0xc3dc0000
	s_mov_b32 s5, 0
	s_sub_i32 s33, s61, s60
	s_sub_i32 s33, s33, s48
	s_add_i32 s33, s33, 1
	s_ashr_i32 s33, s33, 1
	s_waitcnt lgkmcnt(0)
	s_cmp_lt_i32 s33, 1
	s_cbranch_scc1 .Ltg11_done
	s_add_i32 s36, s60, s48
	s_lshl_b32 s57, s33, 1
	s_add_i32 s57, s57, s36
	s_add_i32 s57, s57, -2
	s_waitcnt lgkmcnt(0)
	s_lshr_b32 s56, s36, 12
	s_bfe_u32 s7, s36, 0x60006
	s_add_i32 s7, s7, 64
	s_and_b32 s48, s36, 63
	s_cmp_gt_u32 s56, 1
	s_cbranch_scc1 .Ltg11_d1_down
	s_lshl_b32 s38, s7, 22
	s_lshr_b32 s39, s48, 2
	s_lshl_b32 s49, s39, 18
	s_add_i32 s38, s38, s49
	s_and_b32 s49, s48, 3
	s_lshl_b32 vcc_lo, s49, 9
	s_add_i32 s38, s38, vcc_lo
	s_cmp_eq_u32 s56, 0
	s_cselect_b32 s18, s40, s42
	s_cselect_b32 s19, s41, s43
	s_add_u32 s18, s18, s38
	s_addc_u32 s19, s19, 0
	s_lshl_b32 s38, s7, 21
	s_lshl_b32 vcc_lo, s49, 19
	s_add_i32 s38, s38, vcc_lo
	s_lshl_b32 vcc_lo, s39, 7
	s_add_i32 s38, s38, vcc_lo
	s_lshl_b32 vcc_lo, s56, 14
	s_add_i32 s38, s38, vcc_lo
	s_add_i32 s38, s38, 0x4000000
	s_add_u32 s50, s46, s38
	s_addc_u32 s51, s47, 0
	s_mov_b32 s54, 0
	s_mov_b32 s58, 0x42800000
	s_movk_i32 s49, 0x800
	v_mov_b32_e32 v200, v196
	s_branch .Ltg11_d1_go
.Ltg11_d1_down:
	s_lshl_b32 s38, s7, 22
	s_lshr_b32 s39, s48, 4
	s_lshl_b32 s49, s39, 20
	s_add_i32 s38, s38, s49
	s_and_b32 s49, s48, 15
	s_lshl_b32 vcc_lo, s49, 9
	s_add_i32 s38, s38, vcc_lo
	s_add_u32 s18, s44, s38
	s_addc_u32 s19, s45, 0
	s_lshl_b32 s38, s7, 20
	s_lshl_b32 vcc_lo, s49, 16
	s_add_i32 s38, s38, vcc_lo
	s_lshl_b32 vcc_lo, s39, 7
	s_add_i32 s38, s38, vcc_lo
	s_add_u32 s38, s38, 0x24000000
	s_add_u32 s50, s46, s38
	s_addc_u32 s51, s47, 0
	s_mov_b32 s54, 1
	s_mov_b32 s58, 0x42000000
	s_movk_i32 s49, 0x2000
	v_mov_b32_e32 v200, v197
.Ltg11_d1_go:
	global_load_dwordx4 v[0:3], v200, s[18:19] nt
	s_add_u32 s18, s18, s49
	s_addc_u32 s19, s19, 0
	global_load_dwordx4 v[4:7], v200, s[18:19] nt
	s_add_u32 s18, s18, s49
	s_addc_u32 s19, s19, 0
	global_load_dwordx4 v[8:11], v200, s[18:19] nt
	s_add_u32 s18, s18, s49
	s_addc_u32 s19, s19, 0
	global_load_dwordx4 v[12:15], v200, s[18:19] nt
	s_add_u32 s18, s18, s49
	s_addc_u32 s19, s19, 0
	global_load_dwordx4 v[16:19], v200, s[18:19] nt
	s_add_u32 s18, s18, s49
	s_addc_u32 s19, s19, 0
	global_load_dwordx4 v[20:23], v200, s[18:19] nt
	s_add_u32 s18, s18, s49
	s_addc_u32 s19, s19, 0
	global_load_dwordx4 v[24:27], v200, s[18:19] nt
	s_add_u32 s18, s18, s49
	s_addc_u32 s19, s19, 0
	global_load_dwordx4 v[28:31], v200, s[18:19] nt
	s_add_u32 s18, s18, s49
	s_addc_u32 s19, s19, 0
	global_load_dwordx4 v[32:35], v200, s[18:19] nt
	s_add_u32 s18, s18, s49
	s_addc_u32 s19, s19, 0
	global_load_dwordx4 v[36:39], v200, s[18:19] nt
	s_add_u32 s18, s18, s49
	s_addc_u32 s19, s19, 0
	global_load_dwordx4 v[40:43], v200, s[18:19] nt
	s_add_u32 s18, s18, s49
	s_addc_u32 s19, s19, 0
	global_load_dwordx4 v[44:47], v200, s[18:19] nt
	s_add_u32 s18, s18, s49
	s_addc_u32 s19, s19, 0
	global_load_dwordx4 v[48:51], v200, s[18:19] nt
	s_add_u32 s18, s18, s49
	s_addc_u32 s19, s19, 0
	global_load_dwordx4 v[52:55], v200, s[18:19] nt
	s_add_u32 s18, s18, s49
	s_addc_u32 s19, s19, 0
	global_load_dwordx4 v[56:59], v200, s[18:19] nt
	s_add_u32 s18, s18, s49
	s_addc_u32 s19, s19, 0
	global_load_dwordx4 v[60:63], v200, s[18:19] nt
.Ltg11_loopA:
	s_add_i32 s36, s36, 2
	s_min_i32 s36, s36, s57
	s_lshr_b32 s56, s36, 12
	s_bfe_u32 s7, s36, 0x60006
	s_add_i32 s7, s7, 64
	s_and_b32 s48, s36, 63
	s_cmp_gt_u32 s56, 1
	s_cbranch_scc1 .Ltg11_d2_down
	s_lshl_b32 s38, s7, 22
	s_lshr_b32 s39, s48, 2
	s_lshl_b32 s49, s39, 18
	s_add_i32 s38, s38, s49
	s_and_b32 s49, s48, 3
	s_lshl_b32 vcc_lo, s49, 9
	s_add_i32 s38, s38, vcc_lo
	s_cmp_eq_u32 s56, 0
	s_cselect_b32 s18, s40, s42
	s_cselect_b32 s19, s41, s43
	s_add_u32 s18, s18, s38
	s_addc_u32 s19, s19, 0
	s_lshl_b32 s38, s7, 21
	s_lshl_b32 vcc_lo, s49, 19
	s_add_i32 s38, s38, vcc_lo
	s_lshl_b32 vcc_lo, s39, 7
	s_add_i32 s38, s38, vcc_lo
	s_lshl_b32 vcc_lo, s56, 14
	s_add_i32 s38, s38, vcc_lo
	s_add_i32 s38, s38, 0x4000000
	s_add_u32 s52, s46, s38
	s_addc_u32 s53, s47, 0
	s_mov_b32 s55, 0
	s_mov_b32 s59, 0x42800000
	s_movk_i32 s49, 0x800
	v_mov_b32_e32 v200, v196
	s_branch .Ltg11_d2_go
.Ltg11_d2_down:
	s_lshl_b32 s38, s7, 22
	s_lshr_b32 s39, s48, 4
	s_lshl_b32 s49, s39, 20
	s_add_i32 s38, s38, s49
	s_and_b32 s49, s48, 15
	s_lshl_b32 vcc_lo, s49, 9
	s_add_i32 s38, s38, vcc_lo
	s_add_u32 s18, s44, s38
	s_addc_u32 s19, s45, 0
	s_lshl_b32 s38, s7, 20
	s_lshl_b32 vcc_lo, s49, 16
	s_add_i32 s38, s38, vcc_lo
	s_lshl_b32 vcc_lo, s39, 7
	s_add_i32 s38, s38, vcc_lo
	s_add_u32 s38, s38, 0x24000000
	s_add_u32 s52, s46, s38
	s_addc_u32 s53, s47, 0
	s_mov_b32 s55, 1
	s_mov_b32 s59, 0x42000000
	s_movk_i32 s49, 0x2000
	v_mov_b32_e32 v200, v197
.Ltg11_d2_go:
	global_load_dwordx4 v[64:67], v200, s[18:19] nt
	s_add_u32 s18, s18, s49
	s_addc_u32 s19, s19, 0
	global_load_dwordx4 v[68:71], v200, s[18:19] nt
	s_add_u32 s18, s18, s49
	s_addc_u32 s19, s19, 0
	global_load_dwordx4 v[72:75], v200, s[18:19] nt
	s_add_u32 s18, s18, s49
	s_addc_u32 s19, s19, 0
	global_load_dwordx4 v[76:79], v200, s[18:19] nt
	s_add_u32 s18, s18, s49
	s_addc_u32 s19, s19, 0
	global_load_dwordx4 v[80:83], v200, s[18:19] nt
	s_add_u32 s18, s18, s49
	s_addc_u32 s19, s19, 0
	global_load_dwordx4 v[84:87], v200, s[18:19] nt
	s_add_u32 s18, s18, s49
	s_addc_u32 s19, s19, 0
	global_load_dwordx4 v[88:91], v200, s[18:19] nt
	s_add_u32 s18, s18, s49
	s_addc_u32 s19, s19, 0
	global_load_dwordx4 v[92:95], v200, s[18:19] nt
	s_add_u32 s18, s18, s49
	s_addc_u32 s19, s19, 0
	global_load_dwordx4 v[96:99], v200, s[18:19] nt
	s_add_u32 s18, s18, s49
	s_addc_u32 s19, s19, 0
	global_load_dwordx4 v[100:103], v200, s[18:19] nt
	s_add_u32 s18, s18, s49
	s_addc_u32 s19, s19, 0
	global_load_dwordx4 v[104:107], v200, s[18:19] nt
	s_add_u32 s18, s18, s49
	s_addc_u32 s19, s19, 0
	global_load_dwordx4 v[108:111], v200, s[18:19] nt
	s_add_u32 s18, s18, s49
	s_addc_u32 s19, s19, 0
	global_load_dwordx4 v[112:115], v200, s[18:19] nt
	s_add_u32 s18, s18, s49
	s_addc_u32 s19, s19, 0
	global_load_dwordx4 v[116:119], v200, s[18:19] nt
	s_add_u32 s18, s18, s49
	s_addc_u32 s19, s19, 0
	global_load_dwordx4 v[120:123], v200, s[18:19] nt
	s_add_u32 s18, s18, s49
	s_addc_u32 s19, s19, 0
	global_load_dwordx4 v[124:127], v200, s[18:19] nt
	s_mov_b32 s4, s58
	s_waitcnt vmcnt(28)
	v_pk_mul_f32 v[0:1], v[0:1], s[4:5] op_sel_hi:[1,0]
	v_pk_mul_f32 v[2:3], v[2:3], s[4:5] op_sel_hi:[1,0]
	v_pk_mul_f32 v[4:5], v[4:5], s[4:5] op_sel_hi:[1,0]
	v_pk_mul_f32 v[6:7], v[6:7], s[4:5] op_sel_hi:[1,0]
	v_pk_mul_f32 v[8:9], v[8:9], s[4:5] op_sel_hi:[1,0]
	v_pk_mul_f32 v[10:11], v[10:11], s[4:5] op_sel_hi:[1,0]
	v_pk_mul_f32 v[12:13], v[12:13], s[4:5] op_sel_hi:[1,0]
	v_pk_mul_f32 v[14:15], v[14:15], s[4:5] op_sel_hi:[1,0]
	v_med3_f32 v0, v0, s6, v195
	v_med3_f32 v1, v1, s6, v195
	v_med3_f32 v2, v2, s6, v195
	v_med3_f32 v3, v3, s6, v195
	v_med3_f32 v4, v4, s6, v195
	v_med3_f32 v5, v5, s6, v195
	v_med3_f32 v6, v6, s6, v195
	v_med3_f32 v7, v7, s6, v195
	v_med3_f32 v8, v8, s6, v195
	v_med3_f32 v9, v9, s6, v195
	v_med3_f32 v10, v10, s6, v195
	v_med3_f32 v11, v11, s6, v195
	v_med3_f32 v12, v12, s6, v195
	v_med3_f32 v13, v13, s6, v195
	v_med3_f32 v14, v14, s6, v195
	v_med3_f32 v15, v15, s6, v195
	v_cvt_pk_fp8_f32 v162, v0, v4
	v_cvt_pk_fp8_f32 v166, v1, v5
	v_cvt_pk_fp8_f32 v170, v2, v6
	v_cvt_pk_fp8_f32 v174, v3, v7
	v_cvt_pk_fp8_f32 v162, v8, v12 op_sel:[0,0,1]
	v_cvt_pk_fp8_f32 v166, v9, v13 op_sel:[0,0,1]
	v_cvt_pk_fp8_f32 v170, v10, v14 op_sel:[0,0,1]
	v_cvt_pk_fp8_f32 v174, v11, v15 op_sel:[0,0,1]
	s_waitcnt vmcnt(24)
	v_pk_mul_f32 v[16:17], v[16:17], s[4:5] op_sel_hi:[1,0]
	v_pk_mul_f32 v[18:19], v[18:19], s[4:5] op_sel_hi:[1,0]
	v_pk_mul_f32 v[20:21], v[20:21], s[4:5] op_sel_hi:[1,0]
	v_pk_mul_f32 v[22:23], v[22:23], s[4:5] op_sel_hi:[1,0]
	v_pk_mul_f32 v[24:25], v[24:25], s[4:5] op_sel_hi:[1,0]
	v_pk_mul_f32 v[26:27], v[26:27], s[4:5] op_sel_hi:[1,0]
	v_pk_mul_f32 v[28:29], v[28:29], s[4:5] op_sel_hi:[1,0]
	v_pk_mul_f32 v[30:31], v[30:31], s[4:5] op_sel_hi:[1,0]
	v_med3_f32 v16, v16, s6, v195
	v_med3_f32 v17, v17, s6, v195
	v_med3_f32 v18, v18, s6, v195
	v_med3_f32 v19, v19, s6, v195
	v_med3_f32 v20, v20, s6, v195
	v_med3_f32 v21, v21, s6, v195
	v_med3_f32 v22, v22, s6, v195
	v_med3_f32 v23, v23, s6, v195
	v_med3_f32 v24, v24, s6, v195
	v_med3_f32 v25, v25, s6, v195
	v_med3_f32 v26, v26, s6, v195
	v_med3_f32 v27, v27, s6, v195
	v_med3_f32 v28, v28, s6, v195
	v_med3_f32 v29, v29, s6, v195
	v_med3_f32 v30, v30, s6, v195
	v_med3_f32 v31, v31, s6, v195
	v_cvt_pk_fp8_f32 v163, v16, v20
	v_cvt_pk_fp8_f32 v167, v17, v21
	v_cvt_pk_fp8_f32 v171, v18, v22
	v_cvt_pk_fp8_f32 v175, v19, v23
	v_cvt_pk_fp8_f32 v163, v24, v28 op_sel:[0,0,1]
	v_cvt_pk_fp8_f32 v167, v25, v29 op_sel:[0,0,1]
	v_cvt_pk_fp8_f32 v171, v26, v30 op_sel:[0,0,1]
	v_cvt_pk_fp8_f32 v175, v27, v31 op_sel:[0,0,1]
	s_waitcnt vmcnt(20)
	v_pk_mul_f32 v[32:33], v[32:33], s[4:5] op_sel_hi:[1,0]
	v_pk_mul_f32 v[34:35], v[34:35], s[4:5] op_sel_hi:[1,0]
	v_pk_mul_f32 v[36:37], v[36:37], s[4:5] op_sel_hi:[1,0]
	v_pk_mul_f32 v[38:39], v[38:39], s[4:5] op_sel_hi:[1,0]
	v_pk_mul_f32 v[40:41], v[40:41], s[4:5] op_sel_hi:[1,0]
	v_pk_mul_f32 v[42:43], v[42:43], s[4:5] op_sel_hi:[1,0]
	v_pk_mul_f32 v[44:45], v[44:45], s[4:5] op_sel_hi:[1,0]
	v_pk_mul_f32 v[46:47], v[46:47], s[4:5] op_sel_hi:[1,0]
	v_med3_f32 v32, v32, s6, v195
	v_med3_f32 v33, v33, s6, v195
	v_med3_f32 v34, v34, s6, v195
	v_med3_f32 v35, v35, s6, v195
	v_med3_f32 v36, v36, s6, v195
	v_med3_f32 v37, v37, s6, v195
	v_med3_f32 v38, v38, s6, v195
	v_med3_f32 v39, v39, s6, v195
	v_med3_f32 v40, v40, s6, v195
	v_med3_f32 v41, v41, s6, v195
	v_med3_f32 v42, v42, s6, v195
	v_med3_f32 v43, v43, s6, v195
	v_med3_f32 v44, v44, s6, v195
	v_med3_f32 v45, v45, s6, v195
	v_med3_f32 v46, v46, s6, v195
	v_med3_f32 v47, v47, s6, v195
	v_cvt_pk_fp8_f32 v164, v32, v36
	v_cvt_pk_fp8_f32 v168, v33, v37
	v_cvt_pk_fp8_f32 v172, v34, v38
	v_cvt_pk_fp8_f32 v176, v35, v39
	v_cvt_pk_fp8_f32 v164, v40, v44 op_sel:[0,0,1]
	v_cvt_pk_fp8_f32 v168, v41, v45 op_sel:[0,0,1]
	v_cvt_pk_fp8_f32 v172, v42, v46 op_sel:[0,0,1]
	v_cvt_pk_fp8_f32 v176, v43, v47 op_sel:[0,0,1]
	s_waitcnt vmcnt(16)
	v_pk_mul_f32 v[48:49], v[48:49], s[4:5] op_sel_hi:[1,0]
	v_pk_mul_f32 v[50:51], v[50:51], s[4:5] op_sel_hi:[1,0]
	v_pk_mul_f32 v[52:53], v[52:53], s[4:5] op_sel_hi:[1,0]
	v_pk_mul_f32 v[54:55], v[54:55], s[4:5] op_sel_hi:[1,0]
	v_pk_mul_f32 v[56:57], v[56:57], s[4:5] op_sel_hi:[1,0]
	v_pk_mul_f32 v[58:59], v[58:59], s[4:5] op_sel_hi:[1,0]
	v_pk_mul_f32 v[60:61], v[60:61], s[4:5] op_sel_hi:[1,0]
	v_pk_mul_f32 v[62:63], v[62:63], s[4:5] op_sel_hi:[1,0]
	v_med3_f32 v48, v48, s6, v195
	v_med3_f32 v49, v49, s6, v195
	v_med3_f32 v50, v50, s6, v195
	v_med3_f32 v51, v51, s6, v195
	v_med3_f32 v52, v52, s6, v195
	v_med3_f32 v53, v53, s6, v195
	v_med3_f32 v54, v54, s6, v195
	v_med3_f32 v55, v55, s6, v195
	v_med3_f32 v56, v56, s6, v195
	v_med3_f32 v57, v57, s6, v195
	v_med3_f32 v58, v58, s6, v195
	v_med3_f32 v59, v59, s6, v195
	v_med3_f32 v60, v60, s6, v195
	v_med3_f32 v61, v61, s6, v195
	v_med3_f32 v62, v62, s6, v195
	v_med3_f32 v63, v63, s6, v195
	v_cvt_pk_fp8_f32 v165, v48, v52
	v_cvt_pk_fp8_f32 v169, v49, v53
	v_cvt_pk_fp8_f32 v173, v50, v54
	v_cvt_pk_fp8_f32 v177, v51, v55
	v_cvt_pk_fp8_f32 v165, v56, v60 op_sel:[0,0,1]
	v_cvt_pk_fp8_f32 v169, v57, v61 op_sel:[0,0,1]
	v_cvt_pk_fp8_f32 v173, v58, v62 op_sel:[0,0,1]
	v_cvt_pk_fp8_f32 v177, v59, v63 op_sel:[0,0,1]
	s_lshl_b32 s7, s54, 1
	s_lshr_b32 s7, 0x800, s7
	s_cmp_eq_u32 s54, 0
	v_mov_b32_e32 v201, v198
	s_cbranch_scc1 .Ltg11_p3_st
	v_mov_b32_e32 v201, v199
.Ltg11_p3_st:
	s_mov_b64 s[38:39], s[50:51]
	global_store_dwordx4 v201, v[162:165], s[38:39] nt
	s_add_u32 s38, s38, s7
	s_addc_u32 s39, s39, 0
	global_store_dwordx4 v201, v[166:169], s[38:39] nt
	s_add_u32 s38, s38, s7
	s_addc_u32 s39, s39, 0
	global_store_dwordx4 v201, v[170:173], s[38:39] nt
	s_add_u32 s38, s38, s7
	s_addc_u32 s39, s39, 0
	global_store_dwordx4 v201, v[174:177], s[38:39] nt
	s_add_i32 s33, s33, -1
	s_cmp_eq_u32 s33, 0
	s_cbranch_scc1 .Ltg11_exit
	s_add_i32 s36, s36, 2
	s_min_i32 s36, s36, s57
	s_lshr_b32 s56, s36, 12
	s_bfe_u32 s7, s36, 0x60006
	s_add_i32 s7, s7, 64
	s_and_b32 s48, s36, 63
	s_cmp_gt_u32 s56, 1
	s_cbranch_scc1 .Ltg11_d4_down
	s_lshl_b32 s38, s7, 22
	s_lshr_b32 s39, s48, 2
	s_lshl_b32 s49, s39, 18
	s_add_i32 s38, s38, s49
	s_and_b32 s49, s48, 3
	s_lshl_b32 vcc_lo, s49, 9
	s_add_i32 s38, s38, vcc_lo
	s_cmp_eq_u32 s56, 0
	s_cselect_b32 s18, s40, s42
	s_cselect_b32 s19, s41, s43
	s_add_u32 s18, s18, s38
	s_addc_u32 s19, s19, 0
	s_lshl_b32 s38, s7, 21
	s_lshl_b32 vcc_lo, s49, 19
	s_add_i32 s38, s38, vcc_lo
	s_lshl_b32 vcc_lo, s39, 7
	s_add_i32 s38, s38, vcc_lo
	s_lshl_b32 vcc_lo, s56, 14
	s_add_i32 s38, s38, vcc_lo
	s_add_i32 s38, s38, 0x4000000
	s_add_u32 s50, s46, s38
	s_addc_u32 s51, s47, 0
	s_mov_b32 s54, 0
	s_mov_b32 s58, 0x42800000
	s_movk_i32 s49, 0x800
	v_mov_b32_e32 v200, v196
	s_branch .Ltg11_d4_go

.Ltg11_d4_go:
	global_load_dwordx4 v[0:3], v200, s[18:19] nt
	s_add_u32 s18, s18, s49
	s_addc_u32 s19, s19, 0
	global_load_dwordx4 v[4:7], v200, s[18:19] nt
	s_add_u32 s18, s18, s49
	s_addc_u32 s19, s19, 0
	global_load_dwordx4 v[8:11], v200, s[18:19] nt
	s_add_u32 s18, s18, s49
	s_addc_u32 s19, s19, 0
	global_load_dwordx4 v[12:15], v200, s[18:19] nt
	s_add_u32 s18, s18, s49
	s_addc_u32 s19, s19, 0
	global_load_dwordx4 v[16:19], v200, s[18:19] nt
	s_add_u32 s18, s18, s49
	s_addc_u32 s19, s19, 0
	global_load_dwordx4 v[20:23], v200, s[18:19] nt
	s_add_u32 s18, s18, s49
	s_addc_u32 s19, s19, 0
	global_load_dwordx4 v[24:27], v200, s[18:19] nt
	s_add_u32 s18, s18, s49
	s_addc_u32 s19, s19, 0
	global_load_dwordx4 v[28:31], v200, s[18:19] nt
	s_add_u32 s18, s18, s49
	s_addc_u32 s19, s19, 0
	global_load_dwordx4 v[32:35], v200, s[18:19] nt
	s_add_u32 s18, s18, s49
	s_addc_u32 s19, s19, 0
	global_load_dwordx4 v[36:39], v200, s[18:19] nt
	s_add_u32 s18, s18, s49
	s_addc_u32 s19, s19, 0
	global_load_dwordx4 v[40:43], v200, s[18:19] nt
	s_add_u32 s18, s18, s49
	s_addc_u32 s19, s19, 0
	global_load_dwordx4 v[44:47], v200, s[18:19] nt
	s_add_u32 s18, s18, s49
	s_addc_u32 s19, s19, 0
	global_load_dwordx4 v[48:51], v200, s[18:19] nt
	s_add_u32 s18, s18, s49
	s_addc_u32 s19, s19, 0
	global_load_dwordx4 v[52:55], v200, s[18:19] nt
	s_add_u32 s18, s18, s49
	s_addc_u32 s19, s19, 0
	global_load_dwordx4 v[56:59], v200, s[18:19] nt
	s_add_u32 s18, s18, s49
	s_addc_u32 s19, s19, 0
	global_load_dwordx4 v[60:63], v200, s[18:19] nt
	s_mov_b32 s4, s59
	s_waitcnt vmcnt(28)
	v_pk_mul_f32 v[64:65], v[64:65], s[4:5] op_sel_hi:[1,0]
	v_pk_mul_f32 v[66:67], v[66:67], s[4:5] op_sel_hi:[1,0]
	v_pk_mul_f32 v[68:69], v[68:69], s[4:5] op_sel_hi:[1,0]
	v_pk_mul_f32 v[70:71], v[70:71], s[4:5] op_sel_hi:[1,0]
	v_pk_mul_f32 v[72:73], v[72:73], s[4:5] op_sel_hi:[1,0]
	v_pk_mul_f32 v[74:75], v[74:75], s[4:5] op_sel_hi:[1,0]
	v_pk_mul_f32 v[76:77], v[76:77], s[4:5] op_sel_hi:[1,0]
	v_pk_mul_f32 v[78:79], v[78:79], s[4:5] op_sel_hi:[1,0]
	v_med3_f32 v64, v64, s6, v195
	v_med3_f32 v65, v65, s6, v195
	v_med3_f32 v66, v66, s6, v195
	v_med3_f32 v67, v67, s6, v195
	v_med3_f32 v68, v68, s6, v195
	v_med3_f32 v69, v69, s6, v195
	v_med3_f32 v70, v70, s6, v195
	v_med3_f32 v71, v71, s6, v195
	v_med3_f32 v72, v72, s6, v195
	v_med3_f32 v73, v73, s6, v195
	v_med3_f32 v74, v74, s6, v195
	v_med3_f32 v75, v75, s6, v195
	v_med3_f32 v76, v76, s6, v195
	v_med3_f32 v77, v77, s6, v195
	v_med3_f32 v78, v78, s6, v195
	v_med3_f32 v79, v79, s6, v195
	v_cvt_pk_fp8_f32 v162, v64, v68
	v_cvt_pk_fp8_f32 v166, v65, v69
	v_cvt_pk_fp8_f32 v170, v66, v70
	v_cvt_pk_fp8_f32 v174, v67, v71
	v_cvt_pk_fp8_f32 v162, v72, v76 op_sel:[0,0,1]
	v_cvt_pk_fp8_f32 v166, v73, v77 op_sel:[0,0,1]
	v_cvt_pk_fp8_f32 v170, v74, v78 op_sel:[0,0,1]
	v_cvt_pk_fp8_f32 v174, v75, v79 op_sel:[0,0,1]
	s_waitcnt vmcnt(24)
	v_pk_mul_f32 v[80:81], v[80:81], s[4:5] op_sel_hi:[1,0]
	v_pk_mul_f32 v[82:83], v[82:83], s[4:5] op_sel_hi:[1,0]
	v_pk_mul_f32 v[84:85], v[84:85], s[4:5] op_sel_hi:[1,0]
	v_pk_mul_f32 v[86:87], v[86:87], s[4:5] op_sel_hi:[1,0]
	v_pk_mul_f32 v[88:89], v[88:89], s[4:5] op_sel_hi:[1,0]
	v_pk_mul_f32 v[90:91], v[90:91], s[4:5] op_sel_hi:[1,0]
	v_pk_mul_f32 v[92:93], v[92:93], s[4:5] op_sel_hi:[1,0]
	v_pk_mul_f32 v[94:95], v[94:95], s[4:5] op_sel_hi:[1,0]
	v_med3_f32 v80, v80, s6, v195
	v_med3_f32 v81, v81, s6, v195
	v_med3_f32 v82, v82, s6, v195
	v_med3_f32 v83, v83, s6, v195
	v_med3_f32 v84, v84, s6, v195
	v_med3_f32 v85, v85, s6, v195
	v_med3_f32 v86, v86, s6, v195
	v_med3_f32 v87, v87, s6, v195
	v_med3_f32 v88, v88, s6, v195
	v_med3_f32 v89, v89, s6, v195
	v_med3_f32 v90, v90, s6, v195
	v_med3_f32 v91, v91, s6, v195
	v_med3_f32 v92, v92, s6, v195
	v_med3_f32 v93, v93, s6, v195
	v_med3_f32 v94, v94, s6, v195
	v_med3_f32 v95, v95, s6, v195
	v_cvt_pk_fp8_f32 v163, v80, v84
	v_cvt_pk_fp8_f32 v167, v81, v85
	v_cvt_pk_fp8_f32 v171, v82, v86
	v_cvt_pk_fp8_f32 v175, v83, v87
	v_cvt_pk_fp8_f32 v163, v88, v92 op_sel:[0,0,1]
	v_cvt_pk_fp8_f32 v167, v89, v93 op_sel:[0,0,1]
	v_cvt_pk_fp8_f32 v171, v90, v94 op_sel:[0,0,1]
	v_cvt_pk_fp8_f32 v175, v91, v95 op_sel:[0,0,1]
	s_waitcnt vmcnt(20)
	v_pk_mul_f32 v[96:97], v[96:97], s[4:5] op_sel_hi:[1,0]
	v_pk_mul_f32 v[98:99], v[98:99], s[4:5] op_sel_hi:[1,0]
	v_pk_mul_f32 v[100:101], v[100:101], s[4:5] op_sel_hi:[1,0]
	v_pk_mul_f32 v[102:103], v[102:103], s[4:5] op_sel_hi:[1,0]
	v_pk_mul_f32 v[104:105], v[104:105], s[4:5] op_sel_hi:[1,0]
	v_pk_mul_f32 v[106:107], v[106:107], s[4:5] op_sel_hi:[1,0]
	v_pk_mul_f32 v[108:109], v[108:109], s[4:5] op_sel_hi:[1,0]
	v_pk_mul_f32 v[110:111], v[110:111], s[4:5] op_sel_hi:[1,0]
	v_med3_f32 v96, v96, s6, v195
	v_med3_f32 v97, v97, s6, v195
	v_med3_f32 v98, v98, s6, v195
	v_med3_f32 v99, v99, s6, v195
	v_med3_f32 v100, v100, s6, v195
	v_med3_f32 v101, v101, s6, v195
	v_med3_f32 v102, v102, s6, v195
	v_med3_f32 v103, v103, s6, v195
	v_med3_f32 v104, v104, s6, v195
	v_med3_f32 v105, v105, s6, v195
	v_med3_f32 v106, v106, s6, v195
	v_med3_f32 v107, v107, s6, v195
	v_med3_f32 v108, v108, s6, v195
	v_med3_f32 v109, v109, s6, v195
	v_med3_f32 v110, v110, s6, v195
	v_med3_f32 v111, v111, s6, v195
	v_cvt_pk_fp8_f32 v164, v96, v100
	v_cvt_pk_fp8_f32 v168, v97, v101
	v_cvt_pk_fp8_f32 v172, v98, v102
	v_cvt_pk_fp8_f32 v176, v99, v103
	v_cvt_pk_fp8_f32 v164, v104, v108 op_sel:[0,0,1]
	v_cvt_pk_fp8_f32 v168, v105, v109 op_sel:[0,0,1]
	v_cvt_pk_fp8_f32 v172, v106, v110 op_sel:[0,0,1]
	v_cvt_pk_fp8_f32 v176, v107, v111 op_sel:[0,0,1]
	s_waitcnt vmcnt(16)
	v_pk_mul_f32 v[112:113], v[112:113], s[4:5] op_sel_hi:[1,0]
	v_pk_mul_f32 v[114:115], v[114:115], s[4:5] op_sel_hi:[1,0]
	v_pk_mul_f32 v[116:117], v[116:117], s[4:5] op_sel_hi:[1,0]
	v_pk_mul_f32 v[118:119], v[118:119], s[4:5] op_sel_hi:[1,0]
	v_pk_mul_f32 v[120:121], v[120:121], s[4:5] op_sel_hi:[1,0]
	v_pk_mul_f32 v[122:123], v[122:123], s[4:5] op_sel_hi:[1,0]
	v_pk_mul_f32 v[124:125], v[124:125], s[4:5] op_sel_hi:[1,0]
	v_pk_mul_f32 v[126:127], v[126:127], s[4:5] op_sel_hi:[1,0]
	v_med3_f32 v112, v112, s6, v195
	v_med3_f32 v113, v113, s6, v195
	v_med3_f32 v114, v114, s6, v195
	v_med3_f32 v115, v115, s6, v195
	v_med3_f32 v116, v116, s6, v195
	v_med3_f32 v117, v117, s6, v195
	v_med3_f32 v118, v118, s6, v195
	v_med3_f32 v119, v119, s6, v195
	v_med3_f32 v120, v120, s6, v195
	v_med3_f32 v121, v121, s6, v195
	v_med3_f32 v122, v122, s6, v195
	v_med3_f32 v123, v123, s6, v195
	v_med3_f32 v124, v124, s6, v195
	v_med3_f32 v125, v125, s6, v195
	v_med3_f32 v126, v126, s6, v195
	v_med3_f32 v127, v127, s6, v195
	v_cvt_pk_fp8_f32 v165, v112, v116
	v_cvt_pk_fp8_f32 v169, v113, v117
	v_cvt_pk_fp8_f32 v173, v114, v118
	v_cvt_pk_fp8_f32 v177, v115, v119
	v_cvt_pk_fp8_f32 v165, v120, v124 op_sel:[0,0,1]
	v_cvt_pk_fp8_f32 v169, v121, v125 op_sel:[0,0,1]
	v_cvt_pk_fp8_f32 v173, v122, v126 op_sel:[0,0,1]
	v_cvt_pk_fp8_f32 v177, v123, v127 op_sel:[0,0,1]
	s_lshl_b32 s7, s55, 1
	s_lshr_b32 s7, 0x800, s7
	s_cmp_eq_u32 s55, 0
	v_mov_b32_e32 v201, v198
	s_cbranch_scc1 .Ltg11_p5_st
	v_mov_b32_e32 v201, v199
.Ltg11_p5_st:
	s_mov_b64 s[38:39], s[52:53]
	global_store_dwordx4 v201, v[162:165], s[38:39] nt
	s_add_u32 s38, s38, s7
	s_addc_u32 s39, s39, 0
	global_store_dwordx4 v201, v[166:169], s[38:39] nt
	s_add_u32 s38, s38, s7
	s_addc_u32 s39, s39, 0
	global_store_dwordx4 v201, v[170:173], s[38:39] nt
	s_add_u32 s38, s38, s7
	s_addc_u32 s39, s39, 0
	global_store_dwordx4 v201, v[174:177], s[38:39] nt
	s_add_i32 s33, s33, -1
	s_cmp_lg_u32 s33, 0
	s_cbranch_scc1 .Ltg11_loopA

.Ltg11_done:
	v_readlane_b32 s4, v254, 20
	v_readlane_b32 s5, v254, 21
	v_readlane_b32 s6, v254, 22
	v_readlane_b32 s7, v254, 23
	v_readlane_b32 s18, v254, 24
	v_readlane_b32 s19, v254, 25
	v_readlane_b32 s33, v254, 26
	v_readlane_b32 s36, v254, 27
	v_readlane_b32 s38, v254, 28
	v_readlane_b32 s39, v254, 29
	v_readlane_b32 s40, v254, 30
	v_readlane_b32 s41, v254, 31
	v_readlane_b32 s42, v254, 32
	v_readlane_b32 s43, v254, 33
	v_readlane_b32 s44, v254, 34
	v_readlane_b32 s45, v254, 35
	v_readlane_b32 s46, v254, 36
	v_readlane_b32 s47, v254, 37
	v_readlane_b32 s48, v254, 38
	v_readlane_b32 s49, v254, 39
	v_readlane_b32 s50, v254, 40
	v_readlane_b32 s51, v254, 41
	v_readlane_b32 s52, v254, 42
	v_readlane_b32 s53, v254, 43
	v_readlane_b32 s54, v254, 44
	v_readlane_b32 s55, v254, 45
	v_readlane_b32 s56, v254, 46
	v_readlane_b32 s57, v254, 47
	v_readlane_b32 s58, v254, 48
	v_readlane_b32 s59, v254, 49
	v_readlane_b32 s60, v254, 50
	v_readlane_b32 s61, v254, 51
	s_nop 4

.LBB0_1350:
	s_ashr_i32 s0, s2, 3
	s_mul_hi_i32 s1, s0, 0x66666667
	s_lshr_b32 s4, s1, 31
	s_ashr_i32 s1, s1, 1
	s_add_i32 s1, s1, s4
	s_mul_i32 s1, s1, 5
	s_sub_i32 s69, s0, s1
	s_cmpk_gt_i32 s68, 0x3ff
	s_cselect_b64 s[0:1], -1, 0
	s_cmp_lt_i32 s69, 0
	s_cselect_b64 s[4:5], -1, 0
	s_and_b64 s[0:1], s[0:1], s[4:5]
	s_and_b64 vcc, exec, s[0:1]
	s_cbranch_vccnz .LBB0_1425
	s_load_dwordx2 s[0:1], s[10:11], 0xe8
	v_writelane_b32 v254, s89, 10
	v_writelane_b32 v254, s95, 11
	s_movk_i32 s93, 0xb0
	v_exp_f32_e32 v154, 0xbed49a78
	s_waitcnt lgkmcnt(0)
	s_add_u32 s71, s0, 0x67e00000
	s_addc_u32 s72, s1, 0
	s_add_u32 s73, s0, 0x51600000
	s_addc_u32 s74, s1, 0
	s_add_u32 s75, s0, 0x6ea00000
	s_addc_u32 s76, s1, 0
	s_and_b32 s4, s95, 0xffffffc0
	s_add_i32 s5, s55, 0x1fff
	s_add_u32 s77, s0, 0x24000000
	s_addc_u32 s78, s1, 0
	s_add_u32 s79, s0, 0x4000000
	s_addc_u32 s80, s1, 0
	s_lshl_b32 s0, s3, 8
	s_add_i32 s81, s0, 0
	s_abs_i32 s0, s55
	v_add_u32_e32 v153, s4, v0
	v_cvt_f32_u32_e32 v0, s0
	s_mul_i32 s1, s3, 0x2100
	s_add_i32 s85, s81, s1
	s_xor_b32 s1, s5, s55
	v_rcp_iflag_f32_e32 v0, v0
	s_abs_i32 s4, s5
	s_sub_i32 s5, 0, s0
	s_lshl_b32 s82, s3, 5
	v_mul_f32_e32 v0, 0x4f7ffffe, v0
	v_cvt_u32_f32_e32 v0, v0
	s_and_b32 s83, s82, 32
	s_lshl_b32 s84, s3, 10
	s_lshl_b32 s86, s3, 16
	v_readfirstlane_b32 s6, v0
	s_mul_i32 s5, s5, s6
	s_mul_hi_u32 s5, s6, s5
	s_add_i32 s6, s6, s5
	s_mul_hi_u32 s5, s4, s6
	s_mul_i32 s6, s5, s0
	s_sub_i32 s4, s4, s6
	s_ashr_i32 s1, s1, 31
	s_add_i32 s6, s5, 1
	s_sub_i32 s7, s4, s0
	s_cmp_ge_u32 s4, s0
	s_cselect_b32 s5, s6, s5
	s_cselect_b32 s4, s7, s4
	s_add_i32 s6, s5, 1
	s_cmp_ge_u32 s4, s0
	s_cselect_b32 s0, s6, s5
	s_xor_b32 s0, s0, s1
	s_sub_i32 s0, s0, s1
	s_mul_i32 s87, s0, s68
	s_add_i32 s0, s87, s0
	s_min_i32 s88, s0, 0x2000
	s_cmp_lt_i32 s87, s88
	s_cselect_b64 s[14:15], -1, 0
	s_lshl_b32 s0, s87, 1
	s_and_b32 s0, s0, 0xffffe000
	s_and_b32 s1, s87, 0xfff
	v_writelane_b32 v254, s1, 13
	s_or_b32 s1, s0, s1
	s_bfe_i32 s0, s87, 0x1001e
	s_or_b32 s4, s1, 0x1000
	s_lshr_b32 s0, s0, 19
	s_add_i32 s0, s4, s0
	s_and_b32 s0, s0, 0xffffe000
	s_sub_i32 s0, s4, s0
	s_add_i32 s89, s88, -1
	s_ashr_i32 s0, s0, 6
	s_and_b32 s91, s87, 63
	s_cmpk_gt_i32 s4, 0x3fff
	s_cselect_b64 s[16:17], -1, 0
	s_lshl_b32 s4, s0, 22
	s_addk_i32 s1, 0x2fff
	s_cmpk_lt_u32 s1, 0x3fff
	s_cselect_b32 s1, s93, 0xb8
	v_writelane_b32 v254, s4, 12
	s_add_u32 s4, s10, s1
	s_addc_u32 s5, s11, 0
	s_ashr_i32 s1, s0, 31
	s_lshl_b64 s[20:21], s[0:1], 22
	s_add_i32 s0, s87, 1
	s_min_i32 s94, s0, s89
	s_lshl_b32 s0, s94, 1
	s_and_b32 s0, s0, 0xffffe000
	s_and_b32 s1, s94, 0xfff
	v_writelane_b32 v254, s4, 14
	s_mov_b32 s56, s1
	s_or_b32 s1, s0, s1
	s_bfe_i32 s0, s94, 0x1001e
	v_writelane_b32 v254, s5, 15
	s_or_b32 s4, s1, 0x1000
	s_lshr_b32 s0, s0, 19
	s_add_i32 s0, s4, s0
	s_and_b32 s0, s0, 0xffffe000
	s_sub_i32 s0, s4, s0
	s_ashr_i32 s0, s0, 6
	s_and_b32 s96, s94, 63
	s_cmpk_gt_i32 s4, 0x3fff
	s_cselect_b64 s[24:25], -1, 0
	s_lshl_b32 s4, s0, 22
	s_addk_i32 s1, 0x2fff
	s_cmpk_lt_u32 s1, 0x3fff
	s_cselect_b32 s1, s93, 0xb8
	s_add_u32 s26, s10, s1
	s_addc_u32 s27, s11, 0
	s_ashr_i32 s1, s0, 31
	s_lshl_b64 s[28:29], s[0:1], 22
	s_add_i32 s0, s87, 2
	s_min_i32 s60, s0, s89
	s_lshl_b32 s0, s60, 1
	s_and_b32 s0, s0, 0xffffe000
	s_and_b32 s1, s60, 0xfff
	s_mov_b32 s57, s1
	s_or_b32 s1, s0, s1
	s_bfe_i32 s0, s60, 0x1001e
	v_writelane_b32 v254, s4, 16
	s_or_b32 s4, s1, 0x1000
	s_lshr_b32 s0, s0, 19
	s_add_i32 s0, s4, s0
	s_and_b32 s0, s0, 0xffffe000
	s_sub_i32 s0, s4, s0
	s_ashr_i32 s0, s0, 6
	s_and_b32 s92, s60, 63
	s_cmpk_gt_i32 s4, 0x3fff
	s_cselect_b64 s[30:31], -1, 0
	s_lshl_b32 s4, s0, 22
	s_addk_i32 s1, 0x2fff
	s_cmpk_lt_u32 s1, 0x3fff
	v_exp_f32_e32 v155, 0xbf549a78
	v_exp_f32_e32 v156, 0xbf9f73da
	v_exp_f32_e32 v157, 0xbfd49a78
	v_exp_f32_e32 v158, 0xc004e08b
	v_exp_f32_e32 v159, 0xc01f73da
	v_exp_f32_e32 v160, 0xc03a0729
	v_exp_f32_e32 v161, 0xc0549a78
	v_exp_f32_e32 v162, 0xc06f2dc7
	v_exp_f32_e32 v163, 0xc084e08b
	v_exp_f32_e32 v164, 0xc0922a32
	v_exp_f32_e32 v165, 0xc09f73da
	v_exp_f32_e32 v166, 0xc0acbd82
	v_exp_f32_e32 v167, 0xc0ba0729
	v_exp_f32_e32 v168, 0xc0c750d0
	v_exp_f32_e32 v169, 0xc0d49a78
	v_exp_f32_e32 v170, 0xc0e1e420
	v_exp_f32_e32 v171, 0xc0ef2dc7
	v_exp_f32_e32 v172, 0xc0fc776e
	v_exp_f32_e32 v173, 0xc104e08b
	v_exp_f32_e32 v174, 0xc10b855f
	v_exp_f32_e32 v175, 0xc1122a32
	v_exp_f32_e32 v176, 0xc118cf06
	v_exp_f32_e32 v177, 0xc11f73da
	v_exp_f32_e32 v178, 0xc12618ae
	v_exp_f32_e32 v179, 0xc12cbd82
	v_exp_f32_e32 v180, 0xc1336255
	v_exp_f32_e32 v181, 0xc13a0729
	v_exp_f32_e32 v182, 0xc140abfd
	v_exp_f32_e32 v183, 0xc14750d0
	v_exp_f32_e32 v184, 0xc14df5a4
	s_cselect_b32 s1, s93, 0xb8
	s_add_u32 s34, s10, s1
	s_addc_u32 s35, s11, 0
	s_ashr_i32 s1, s0, 31
	s_mov_b32 s13, 0
	s_lshl_b64 s[52:53], s[0:1], 22
	v_mov_b32_e32 v145, 0
	s_mov_b32 s97, 0xc3dc0000
	s_mov_b32 s22, 0x42b504f3
	s_mov_b32 s54, 0x3e0293ee
	s_movk_i32 s23, 0x110
	v_mov_b32_e32 v185, 0x43dc0000
	v_mov_b32_e32 v186, 0xf149f2ca
	s_mov_b32 s90, 0
	v_writelane_b32 v254, s4, 17
	s_branch .LBB0_1354
